# P5 GLU epilogue: gate clamp min(g,7) through the dequant pk_fma [0,1] clamp modifier (g4 mapped from [-64,28]; below -64 the fp8 output is zero either way), one pk_fma per pair instead of two v_max
# speedup vs baseline: 1.0032x; 1.0032x over previous
.LBB0_555:
	v_and_b32_e32 v6, 15, v4
	s_lshl_b32 s5, s5, 5
	v_lshlrev_b32_e32 v7, 7, v6
	s_and_b32 s5, s5, 0x60
	v_lshl_or_b32 v7, s22, 13, v7
	s_add_u32 s22, s44, 0x80
	v_or_b32_e32 v6, s5, v6
	s_waitcnt vmcnt(2)
	s_barrier
	s_addc_u32 s23, s45, 0
	s_add_i32 s55, s29, 0x18000
	s_mov_b32 m0, s55
	s_nop 0
	global_load_lds_dwordx4 v1, s[22:23] offset:0
	s_add_i32 s56, s29, 0x1a000
	s_mov_b32 m0, s56
	s_nop 0
	global_load_lds_dwordx4 v173, s[22:23] offset:0
	s_add_u32 s22, s18, 0x80
	s_addc_u32 s23, s19, 0
	s_add_i32 s57, s29, 0x8000
	s_mov_b32 m0, s57
	s_nop 0
	global_load_lds_dwordx4 v171, s[22:23] offset:0
	s_add_i32 s58, s29, 0xa000
	s_mov_b32 m0, s58
	s_nop 0
	global_load_lds_dwordx4 v174, s[22:23] offset:0
	s_add_u32 s24, s44, 0x20080
	s_addc_u32 s25, s45, 0
	s_add_i32 s59, s29, 0x1c000
	s_mov_b32 m0, s59
	s_nop 0
	global_load_lds_dwordx4 v1, s[24:25] offset:0
	s_add_i32 s60, s29, 0x1e000
	s_add_i32 s61, s29, 0xc000
	v_bfe_u32 v8, v4, 4, 2
	v_bfe_u32 v4, v4, 1, 3
	s_mov_b32 m0, s60
	s_nop 0
	global_load_lds_dwordx4 v173, s[24:25] offset:0
	s_add_u32 s24, s18, 0x380
	v_bitop3_b32 v5, v5, v4, 3 bitop3:0x6c
	v_bitop3_b32 v4, v8, v4, 4 bitop3:0x36
	s_addc_u32 s25, s19, 0
	v_lshlrev_b32_e32 v5, 4, v5
	v_lshlrev_b32_e32 v4, 4, v4
	v_lshlrev_b32_e32 v6, 7, v6
	s_cmpk_lt_u32 s4, 0x100
	v_and_b32_e32 v3, 0x1000, v3
	s_movk_i32 s4, 0x1f0
	v_or_b32_e32 v176, v6, v5
	v_or_b32_e32 v177, v6, v4
	s_waitcnt vmcnt(6)
	s_cselect_b64 s[26:27], -1, 0
	v_and_or_b32 v178, v2, s4, v3
	s_add_i32 s4, 0, 0x10000
	v_or_b32_e32 v9, v5, v7
	v_or_b32_e32 v7, v4, v7
	v_add_u32_e32 v179, s4, v176
	v_add_u32_e32 v180, s4, v177
	s_add_i32 s4, 0, 0x14000
	s_add_i32 s62, s29, 0xe000
	v_add_u32_e32 v181, s4, v176
	v_add_u32_e32 v182, s4, v177
	v_add_u32_e32 v183, 0, v9
	v_add_u32_e32 v184, 0, v7
	v_mov_b32_e32 v185, 0x7f7f7f7f
	s_movk_i32 s63, 0xffc0
	v_mov_b32_e32 v163, 0
	s_mov_b32 s96, 0xbf1d265f
	s_mov_b32 s98, 0x36b21643
	s_mov_b32 s100, 0x3d321643
	s_mov_b32 s76, 0xc261e729
	v_mov_b32_e32 v228, 0x3f321643
	v_mov_b32_e32 v230, 0x421d265f
	s_mov_b32 s74, 0x37124925
	s_mov_b32 s72, 0x3d924925
	s_mov_b32 s64, 0x41600000
	v_mov_b32_e32 v186, 0xc0c00000
	s_barrier
	s_branch .LBB0_558

.LBB0_566:
	s_lshl_b32 s35, s67, 10
	v_mov_b32_e32 v25, v0
	s_and_b32 s35, s35, 0x400
	s_add_i32 s35, s35, 0
	v_lshrrev_b32_e32 v26, 1, v25
	v_and_b32_e32 v162, 0x60, v26
	v_lshlrev_b32_e32 v3, 1, v25
	s_add_i32 s35, s35, 0x24cc0
	v_lshlrev_b32_e32 v2, 2, v162
	v_and_b32_e32 v3, 0x60, v3
	v_add3_u32 v14, s35, v2, v3
	ds_read_b128 v[2:5], v14
	ds_read_b128 v[6:9], v14 offset:512
	ds_read_b128 v[10:13], v14 offset:16
	v_ashrrev_i32_e32 v24, 2, v25
	s_lshl_b32 s35, s40, 10
	s_lshl_b32 s38, s38, 7
	s_waitcnt lgkmcnt(2)
	v_pk_fma_f32 v[16:17], v[4:5], s[100:101], v[228:229] op_sel_hi:[1,0,0]
	v_pk_fma_f32 v[18:19], v[2:3], s[100:101], v[228:229] op_sel_hi:[1,0,0]
	ds_read_b128 v[2:5], v14 offset:528
	s_waitcnt lgkmcnt(2)
	v_pk_fma_f32 v[20:21], v[8:9], s[72:73], 0.5 op_sel_hi:[1,0,0]
	s_waitcnt lgkmcnt(1)
	v_pk_fma_f32 v[8:9], v[12:13], s[100:101], v[228:229] op_sel_hi:[1,0,0]
	v_pk_fma_f32 v[22:23], v[6:7], s[72:73], 0.5 op_sel_hi:[1,0,0]
	v_and_b32_e32 v6, 16, v26
	s_waitcnt lgkmcnt(0)
	v_pk_fma_f32 v[14:15], v[2:3], s[72:73], 0.5 op_sel_hi:[1,0,0]
	v_and_b32_e32 v2, 15, v25
	v_pk_fma_f32 v[12:13], v[4:5], s[72:73], 0.5 op_sel_hi:[1,0,0]
	v_and_or_b32 v2, v24, s63, v2
	v_pk_fma_f32 v[4:5], v[158:159], s[98:99], v[18:19] op_sel_hi:[1,0,1] clamp
	v_lshl_add_u32 v24, s37, 8, v2
	v_pk_fma_f32 v[2:3], v[160:161], s[98:99], v[16:17] op_sel_hi:[1,0,1] clamp
	v_pk_fma_f32 v[4:5], v[4:5], s[76:77], v[230:231] op_sel_hi:[1,0,0]
	v_pk_fma_f32 v[30:31], v[2:3], s[76:77], v[230:231] op_sel_hi:[1,0,0]
	v_exp_f32_e32 v2, v4
	v_exp_f32_e32 v3, v5
	v_exp_f32_e32 v32, v30
	v_exp_f32_e32 v33, v31
	v_pk_fma_f32 v[2:3], v[2:3], s[96:97], s[96:97] op_sel_hi:[1,0,0]
	v_pk_fma_f32 v[28:29], v[154:155], s[74:75], v[22:23] op_sel_hi:[1,0,1] clamp
	v_rcp_f32_e32 v2, v2
	v_rcp_f32_e32 v3, v3
	v_pk_fma_f32 v[28:29], v[28:29], s[64:65], v[186:187] op_sel_hi:[1,0,0]
	v_pk_fma_f32 v[32:33], v[32:33], s[96:97], s[96:97] op_sel_hi:[1,0,0]
	v_pk_mul_f32 v[4:5], v[4:5], v[28:29]
	v_rcp_f32_e32 v32, v32
	v_rcp_f32_e32 v33, v33
	v_pk_mul_f32 v[4:5], v[4:5], v[2:3]
	v_pk_fma_f32 v[26:27], v[156:157], s[74:75], v[20:21] op_sel_hi:[1,0,1] clamp
	v_cvt_pk_fp8_f32 v2, v4, v5
	v_pk_fma_f32 v[26:27], v[26:27], s[64:65], v[186:187] op_sel_hi:[1,0,0]
	v_pk_mul_f32 v[4:5], v[30:31], v[26:27]
	v_pk_fma_f32 v[10:11], v[10:11], s[100:101], v[228:229] op_sel_hi:[1,0,0]
	v_pk_mul_f32 v[4:5], v[4:5], v[32:33]
	v_pk_fma_f32 v[26:27], v[150:151], s[98:99], v[10:11] op_sel_hi:[1,0,1] clamp
	v_cvt_pk_fp8_f32 v2, v4, v5 op_sel:[0,0,1]
	v_pk_fma_f32 v[4:5], v[152:153], s[98:99], v[8:9] op_sel_hi:[1,0,1] clamp
	v_pk_fma_f32 v[26:27], v[26:27], s[76:77], v[230:231] op_sel_hi:[1,0,0]
	v_pk_fma_f32 v[4:5], v[4:5], s[76:77], v[230:231] op_sel_hi:[1,0,0]
	v_pk_fma_f32 v[30:31], v[146:147], s[74:75], v[14:15] op_sel_hi:[1,0,1] clamp
	v_exp_f32_e32 v32, v26
	v_exp_f32_e32 v146, v4
	v_exp_f32_e32 v147, v5
	v_exp_f32_e32 v33, v27
	v_pk_fma_f32 v[30:31], v[30:31], s[64:65], v[186:187] op_sel_hi:[1,0,0]
	v_pk_fma_f32 v[146:147], v[146:147], s[96:97], s[96:97] op_sel_hi:[1,0,0]
	v_pk_fma_f32 v[32:33], v[32:33], s[96:97], s[96:97] op_sel_hi:[1,0,0]
	v_pk_mul_f32 v[26:27], v[26:27], v[30:31]
	v_rcp_f32_e32 v32, v32
	v_rcp_f32_e32 v33, v33
	v_rcp_f32_e32 v146, v146
	v_rcp_f32_e32 v147, v147
	v_pk_mul_f32 v[26:27], v[26:27], v[32:33]
	v_pk_fma_f32 v[28:29], v[148:149], s[74:75], v[12:13] op_sel_hi:[1,0,1] clamp
	v_cvt_pk_fp8_f32 v3, v26, v27
	v_pk_fma_f32 v[28:29], v[28:29], s[64:65], v[186:187] op_sel_hi:[1,0,0]
	v_pk_mul_f32 v[4:5], v[4:5], v[28:29]
	v_pk_fma_f32 v[26:27], v[142:143], s[98:99], v[18:19] op_sel_hi:[1,0,1] clamp
	v_pk_mul_f32 v[4:5], v[4:5], v[146:147]
	v_pk_fma_f32 v[26:27], v[26:27], s[76:77], v[230:231] op_sel_hi:[1,0,0]
	v_cvt_pk_fp8_f32 v3, v4, v5 op_sel:[0,0,1]
	v_pk_fma_f32 v[4:5], v[144:145], s[98:99], v[16:17] op_sel_hi:[1,0,1] clamp
	v_pk_fma_f32 v[32:33], v[4:5], s[76:77], v[230:231] op_sel_hi:[1,0,0]
	v_exp_f32_e32 v4, v26
	v_exp_f32_e32 v5, v27
	v_pk_fma_f32 v[30:31], v[138:139], s[74:75], v[22:23] op_sel_hi:[1,0,1] clamp
	v_exp_f32_e32 v138, v32
	v_exp_f32_e32 v139, v33
	v_pk_fma_f32 v[4:5], v[4:5], s[96:97], s[96:97] op_sel_hi:[1,0,0]
	v_pk_fma_f32 v[30:31], v[30:31], s[64:65], v[186:187] op_sel_hi:[1,0,0]
	v_rcp_f32_e32 v4, v4
	v_rcp_f32_e32 v5, v5
	v_pk_fma_f32 v[138:139], v[138:139], s[96:97], s[96:97] op_sel_hi:[1,0,0]
	v_pk_mul_f32 v[26:27], v[26:27], v[30:31]
	v_rcp_f32_e32 v138, v138
	v_rcp_f32_e32 v139, v139
	v_pk_mul_f32 v[26:27], v[26:27], v[4:5]
	v_pk_fma_f32 v[28:29], v[140:141], s[74:75], v[20:21] op_sel_hi:[1,0,1] clamp
	v_cvt_pk_fp8_f32 v4, v26, v27
	v_pk_fma_f32 v[28:29], v[28:29], s[64:65], v[186:187] op_sel_hi:[1,0,0]
	v_pk_mul_f32 v[26:27], v[32:33], v[28:29]
	v_pk_fma_f32 v[28:29], v[134:135], s[98:99], v[10:11] op_sel_hi:[1,0,1] clamp
	v_pk_mul_f32 v[26:27], v[26:27], v[138:139]
	v_pk_fma_f32 v[28:29], v[28:29], s[76:77], v[230:231] op_sel_hi:[1,0,0]
	v_cvt_pk_fp8_f32 v4, v26, v27 op_sel:[0,0,1]
	v_pk_fma_f32 v[26:27], v[136:137], s[98:99], v[8:9] op_sel_hi:[1,0,1] clamp
	v_pk_fma_f32 v[32:33], v[130:131], s[74:75], v[14:15] op_sel_hi:[1,0,1] clamp
	v_pk_fma_f32 v[26:27], v[26:27], s[76:77], v[230:231] op_sel_hi:[1,0,0]
	v_pk_fma_f32 v[30:31], v[132:133], s[74:75], v[12:13] op_sel_hi:[1,0,1] clamp
	v_exp_f32_e32 v130, v28
	v_exp_f32_e32 v132, v26
	v_exp_f32_e32 v133, v27
	v_exp_f32_e32 v131, v29
	v_pk_fma_f32 v[32:33], v[32:33], s[64:65], v[186:187] op_sel_hi:[1,0,0]
	v_pk_fma_f32 v[132:133], v[132:133], s[96:97], s[96:97] op_sel_hi:[1,0,0]
	v_pk_fma_f32 v[130:131], v[130:131], s[96:97], s[96:97] op_sel_hi:[1,0,0]
	v_pk_mul_f32 v[28:29], v[28:29], v[32:33]
	v_rcp_f32_e32 v130, v130
	v_rcp_f32_e32 v131, v131
	v_rcp_f32_e32 v132, v132
	v_rcp_f32_e32 v133, v133
	v_pk_mul_f32 v[28:29], v[28:29], v[130:131]
	v_pk_fma_f32 v[30:31], v[30:31], s[64:65], v[186:187] op_sel_hi:[1,0,0]
	v_cvt_pk_fp8_f32 v5, v28, v29
	v_pk_fma_f32 v[28:29], v[126:127], s[98:99], v[18:19] op_sel_hi:[1,0,1] clamp
	v_pk_fma_f32 v[28:29], v[28:29], s[76:77], v[230:231] op_sel_hi:[1,0,0]
	v_pk_mul_f32 v[26:27], v[26:27], v[30:31]
	v_pk_fma_f32 v[32:33], v[122:123], s[74:75], v[22:23] op_sel_hi:[1,0,1] clamp
	v_pk_mul_f32 v[26:27], v[26:27], v[132:133]
	v_exp_f32_e32 v122, v28
	v_exp_f32_e32 v123, v29
	v_cvt_pk_fp8_f32 v5, v26, v27 op_sel:[0,0,1]
	v_pk_fma_f32 v[26:27], v[128:129], s[98:99], v[16:17] op_sel_hi:[1,0,1] clamp
	v_pk_fma_f32 v[30:31], v[124:125], s[74:75], v[20:21] op_sel_hi:[1,0,1] clamp
	v_pk_fma_f32 v[26:27], v[26:27], s[76:77], v[230:231] op_sel_hi:[1,0,0]
	v_exp_f32_e32 v124, v26
	v_exp_f32_e32 v125, v27
	v_pk_fma_f32 v[122:123], v[122:123], s[96:97], s[96:97] op_sel_hi:[1,0,0]
	v_pk_fma_f32 v[32:33], v[32:33], s[64:65], v[186:187] op_sel_hi:[1,0,0]
	v_rcp_f32_e32 v122, v122
	v_rcp_f32_e32 v123, v123
	v_pk_fma_f32 v[124:125], v[124:125], s[96:97], s[96:97] op_sel_hi:[1,0,0]
	v_pk_mul_f32 v[28:29], v[28:29], v[32:33]
	v_rcp_f32_e32 v124, v124
	v_rcp_f32_e32 v125, v125
	v_pk_mul_f32 v[32:33], v[28:29], v[122:123]
	v_cvt_pk_fp8_f32 v28, v32, v33
	v_pk_fma_f32 v[30:31], v[30:31], s[64:65], v[186:187] op_sel_hi:[1,0,0]
	v_pk_mul_f32 v[26:27], v[26:27], v[30:31]
	v_pk_fma_f32 v[30:31], v[118:119], s[98:99], v[10:11] op_sel_hi:[1,0,1] clamp
	v_pk_mul_f32 v[26:27], v[26:27], v[124:125]
	v_pk_fma_f32 v[30:31], v[30:31], s[76:77], v[230:231] op_sel_hi:[1,0,0]
	v_cvt_pk_fp8_f32 v28, v26, v27 op_sel:[0,0,1]
	v_pk_fma_f32 v[26:27], v[120:121], s[98:99], v[8:9] op_sel_hi:[1,0,1] clamp
	v_pk_fma_f32 v[32:33], v[116:117], s[74:75], v[12:13] op_sel_hi:[1,0,1] clamp
	v_pk_fma_f32 v[26:27], v[26:27], s[76:77], v[230:231] op_sel_hi:[1,0,0]
	v_exp_f32_e32 v116, v30
	v_exp_f32_e32 v118, v26
	v_exp_f32_e32 v119, v27
	v_exp_f32_e32 v117, v31
	v_pk_fma_f32 v[114:115], v[114:115], s[74:75], v[14:15] op_sel_hi:[1,0,1] clamp
	v_pk_fma_f32 v[114:115], v[114:115], s[64:65], v[186:187] op_sel_hi:[1,0,0]
	v_pk_fma_f32 v[116:117], v[116:117], s[96:97], s[96:97] op_sel_hi:[1,0,0]
	v_rcp_f32_e32 v116, v116
	v_rcp_f32_e32 v117, v117
	v_pk_fma_f32 v[118:119], v[118:119], s[96:97], s[96:97] op_sel_hi:[1,0,0]
	v_pk_mul_f32 v[30:31], v[30:31], v[114:115]
	v_rcp_f32_e32 v118, v118
	v_rcp_f32_e32 v119, v119
	v_pk_mul_f32 v[30:31], v[30:31], v[116:117]
	v_pk_fma_f32 v[32:33], v[32:33], s[64:65], v[186:187] op_sel_hi:[1,0,0]
	v_cvt_pk_fp8_f32 v29, v30, v31
	v_pk_fma_f32 v[30:31], v[110:111], s[98:99], v[18:19] op_sel_hi:[1,0,1] clamp
	v_pk_fma_f32 v[30:31], v[30:31], s[76:77], v[230:231] op_sel_hi:[1,0,0]
	v_pk_mul_f32 v[26:27], v[26:27], v[32:33]
	v_pk_fma_f32 v[32:33], v[108:109], s[74:75], v[20:21] op_sel_hi:[1,0,1] clamp
	v_pk_mul_f32 v[26:27], v[26:27], v[118:119]
	v_exp_f32_e32 v108, v30
	v_exp_f32_e32 v109, v31
	v_cvt_pk_fp8_f32 v29, v26, v27 op_sel:[0,0,1]
	v_pk_fma_f32 v[26:27], v[112:113], s[98:99], v[16:17] op_sel_hi:[1,0,1] clamp
	v_pk_fma_f32 v[106:107], v[106:107], s[74:75], v[22:23] op_sel_hi:[1,0,1] clamp
	v_pk_fma_f32 v[26:27], v[26:27], s[76:77], v[230:231] op_sel_hi:[1,0,0]
	v_exp_f32_e32 v110, v26
	v_exp_f32_e32 v111, v27
	v_pk_fma_f32 v[108:109], v[108:109], s[96:97], s[96:97] op_sel_hi:[1,0,0]
	v_pk_fma_f32 v[106:107], v[106:107], s[64:65], v[186:187] op_sel_hi:[1,0,0]
	v_rcp_f32_e32 v108, v108
	v_rcp_f32_e32 v109, v109
	v_pk_fma_f32 v[110:111], v[110:111], s[96:97], s[96:97] op_sel_hi:[1,0,0]
	v_pk_mul_f32 v[30:31], v[30:31], v[106:107]
	v_rcp_f32_e32 v110, v110
	v_rcp_f32_e32 v111, v111
	v_pk_mul_f32 v[106:107], v[30:31], v[108:109]
	v_cvt_pk_fp8_f32 v30, v106, v107
	v_pk_fma_f32 v[32:33], v[32:33], s[64:65], v[186:187] op_sel_hi:[1,0,0]
	v_pk_mul_f32 v[26:27], v[26:27], v[32:33]
	v_pk_fma_f32 v[32:33], v[102:103], s[98:99], v[10:11] op_sel_hi:[1,0,1] clamp
	v_pk_mul_f32 v[26:27], v[26:27], v[110:111]
	v_pk_fma_f32 v[32:33], v[32:33], s[76:77], v[230:231] op_sel_hi:[1,0,0]
	v_cvt_pk_fp8_f32 v30, v26, v27 op_sel:[0,0,1]
	v_pk_fma_f32 v[26:27], v[104:105], s[98:99], v[8:9] op_sel_hi:[1,0,1] clamp
	v_pk_fma_f32 v[26:27], v[26:27], s[76:77], v[230:231] op_sel_hi:[1,0,0]
	v_exp_f32_e32 v102, v32
	v_exp_f32_e32 v104, v26
	v_exp_f32_e32 v105, v27
	v_exp_f32_e32 v103, v33
	v_pk_fma_f32 v[98:99], v[98:99], s[74:75], v[14:15] op_sel_hi:[1,0,1] clamp
	v_pk_fma_f32 v[98:99], v[98:99], s[64:65], v[186:187] op_sel_hi:[1,0,0]
	v_pk_fma_f32 v[102:103], v[102:103], s[96:97], s[96:97] op_sel_hi:[1,0,0]
	v_rcp_f32_e32 v102, v102
	v_rcp_f32_e32 v103, v103
	v_pk_fma_f32 v[104:105], v[104:105], s[96:97], s[96:97] op_sel_hi:[1,0,0]
	v_pk_mul_f32 v[32:33], v[32:33], v[98:99]
	v_rcp_f32_e32 v104, v104
	v_rcp_f32_e32 v105, v105
	v_pk_mul_f32 v[32:33], v[32:33], v[102:103]
	v_pk_fma_f32 v[100:101], v[100:101], s[74:75], v[12:13] op_sel_hi:[1,0,1] clamp
	v_cvt_pk_fp8_f32 v31, v32, v33
	v_pk_fma_f32 v[100:101], v[100:101], s[64:65], v[186:187] op_sel_hi:[1,0,0]
	v_pk_mul_f32 v[26:27], v[26:27], v[100:101]
	v_and_b32_e32 v25, 16, v25
	v_pk_mul_f32 v[26:27], v[26:27], v[104:105]
	s_sub_i32 s38, s38, s35
	v_cvt_pk_fp8_f32 v31, v26, v27 op_sel:[0,0,1]
	v_or_b32_e32 v26, v24, v25
	v_ashrrev_i32_e32 v27, 31, v26
	v_lshlrev_b64 v[26:27], 10, v[26:27]
	s_ashr_i32 s39, s38, 31
	v_lshl_add_u64 v[26:27], s[12:13], 0, v[26:27]
	v_lshl_add_u64 v[26:27], v[26:27], 0, s[38:39]
	v_mov_b32_e32 v7, v163
	v_lshl_add_u64 v[26:27], v[26:27], 0, v[162:163]
	v_permlane16_swap_b32_e32 v2, v4
	v_permlane16_swap_b32_e32 v3, v5
	v_lshl_add_u64 v[26:27], v[26:27], 0, v[6:7]
	global_store_dwordx4 v[26:27], v[2:5], off
	v_or_b32_e32 v26, 32, v25
	v_permlane16_swap_b32_e32 v28, v30
	v_or_b32_e32 v2, v24, v26
	v_ashrrev_i32_e32 v3, 31, v2
	v_lshlrev_b64 v[2:3], 10, v[2:3]
	v_lshl_add_u64 v[2:3], s[12:13], 0, v[2:3]
	v_lshl_add_u64 v[2:3], v[2:3], 0, s[38:39]
	v_lshl_add_u64 v[2:3], v[2:3], 0, v[162:163]
	v_permlane16_swap_b32_e32 v29, v31
	v_lshl_add_u64 v[2:3], v[2:3], 0, v[6:7]
	v_pk_fma_f32 v[4:5], v[94:95], s[98:99], v[18:19] op_sel_hi:[1,0,1] clamp
	global_store_dwordx4 v[2:3], v[28:31], off
	v_pk_fma_f32 v[2:3], v[96:97], s[98:99], v[16:17] op_sel_hi:[1,0,1] clamp
	v_pk_fma_f32 v[4:5], v[4:5], s[76:77], v[230:231] op_sel_hi:[1,0,0]
	v_pk_fma_f32 v[32:33], v[2:3], s[76:77], v[230:231] op_sel_hi:[1,0,0]
	v_exp_f32_e32 v2, v4
	v_exp_f32_e32 v3, v5
	v_pk_fma_f32 v[30:31], v[90:91], s[74:75], v[22:23] op_sel_hi:[1,0,1] clamp
	v_exp_f32_e32 v90, v32
	v_exp_f32_e32 v91, v33
	v_pk_fma_f32 v[2:3], v[2:3], s[96:97], s[96:97] op_sel_hi:[1,0,0]
	v_pk_fma_f32 v[30:31], v[30:31], s[64:65], v[186:187] op_sel_hi:[1,0,0]
	v_rcp_f32_e32 v2, v2
	v_rcp_f32_e32 v3, v3
	v_pk_fma_f32 v[28:29], v[92:93], s[74:75], v[20:21] op_sel_hi:[1,0,1] clamp
	v_pk_fma_f32 v[90:91], v[90:91], s[96:97], s[96:97] op_sel_hi:[1,0,0]
	v_pk_mul_f32 v[4:5], v[4:5], v[30:31]
	v_pk_fma_f32 v[28:29], v[28:29], s[64:65], v[186:187] op_sel_hi:[1,0,0]
	v_rcp_f32_e32 v90, v90
	v_rcp_f32_e32 v91, v91
	v_pk_mul_f32 v[4:5], v[4:5], v[2:3]
	v_cvt_pk_fp8_f32 v2, v4, v5
	v_pk_mul_f32 v[4:5], v[32:33], v[28:29]
	v_pk_fma_f32 v[28:29], v[86:87], s[98:99], v[10:11] op_sel_hi:[1,0,1] clamp
	v_pk_mul_f32 v[4:5], v[4:5], v[90:91]
	v_pk_fma_f32 v[28:29], v[28:29], s[76:77], v[230:231] op_sel_hi:[1,0,0]
	v_pk_fma_f32 v[32:33], v[82:83], s[74:75], v[14:15] op_sel_hi:[1,0,1] clamp
	v_exp_f32_e32 v82, v28
	v_cvt_pk_fp8_f32 v2, v4, v5 op_sel:[0,0,1]
	v_pk_fma_f32 v[4:5], v[88:89], s[98:99], v[8:9] op_sel_hi:[1,0,1] clamp
	v_exp_f32_e32 v83, v29
	v_pk_fma_f32 v[4:5], v[4:5], s[76:77], v[230:231] op_sel_hi:[1,0,0]
	v_pk_fma_f32 v[30:31], v[84:85], s[74:75], v[12:13] op_sel_hi:[1,0,1] clamp
	v_exp_f32_e32 v84, v4
	v_exp_f32_e32 v85, v5
	v_pk_fma_f32 v[82:83], v[82:83], s[96:97], s[96:97] op_sel_hi:[1,0,0]
	v_pk_fma_f32 v[32:33], v[32:33], s[64:65], v[186:187] op_sel_hi:[1,0,0]
	v_rcp_f32_e32 v82, v82
	v_rcp_f32_e32 v83, v83
	v_pk_fma_f32 v[84:85], v[84:85], s[96:97], s[96:97] op_sel_hi:[1,0,0]
	v_pk_mul_f32 v[28:29], v[28:29], v[32:33]
	v_rcp_f32_e32 v84, v84
	v_rcp_f32_e32 v85, v85
	v_pk_mul_f32 v[28:29], v[28:29], v[82:83]
	v_cvt_pk_fp8_f32 v3, v28, v29
	v_pk_fma_f32 v[30:31], v[30:31], s[64:65], v[186:187] op_sel_hi:[1,0,0]
	v_pk_mul_f32 v[4:5], v[4:5], v[30:31]
	v_pk_fma_f32 v[28:29], v[78:79], s[98:99], v[18:19] op_sel_hi:[1,0,1] clamp
	v_pk_mul_f32 v[4:5], v[4:5], v[84:85]
	v_pk_fma_f32 v[28:29], v[28:29], s[76:77], v[230:231] op_sel_hi:[1,0,0]
	v_cvt_pk_fp8_f32 v3, v4, v5 op_sel:[0,0,1]
	v_pk_fma_f32 v[4:5], v[80:81], s[98:99], v[16:17] op_sel_hi:[1,0,1] clamp
	v_pk_fma_f32 v[32:33], v[74:75], s[74:75], v[22:23] op_sel_hi:[1,0,1] clamp
	v_pk_fma_f32 v[74:75], v[4:5], s[76:77], v[230:231] op_sel_hi:[1,0,0]
	v_exp_f32_e32 v4, v28
	v_exp_f32_e32 v5, v29
	v_pk_fma_f32 v[30:31], v[76:77], s[74:75], v[20:21] op_sel_hi:[1,0,1] clamp
	v_exp_f32_e32 v76, v74
	v_exp_f32_e32 v77, v75
	v_pk_fma_f32 v[4:5], v[4:5], s[96:97], s[96:97] op_sel_hi:[1,0,0]
	v_pk_fma_f32 v[32:33], v[32:33], s[64:65], v[186:187] op_sel_hi:[1,0,0]
	v_rcp_f32_e32 v4, v4
	v_rcp_f32_e32 v5, v5
	v_pk_fma_f32 v[76:77], v[76:77], s[96:97], s[96:97] op_sel_hi:[1,0,0]
	v_pk_mul_f32 v[28:29], v[28:29], v[32:33]
	v_pk_fma_f32 v[30:31], v[30:31], s[64:65], v[186:187] op_sel_hi:[1,0,0]
	v_rcp_f32_e32 v76, v76
	v_rcp_f32_e32 v77, v77
	v_pk_mul_f32 v[28:29], v[28:29], v[4:5]
	v_cvt_pk_fp8_f32 v4, v28, v29
	v_pk_mul_f32 v[28:29], v[74:75], v[30:31]
	v_pk_fma_f32 v[30:31], v[70:71], s[98:99], v[10:11] op_sel_hi:[1,0,1] clamp
	v_pk_mul_f32 v[28:29], v[28:29], v[76:77]
	v_pk_fma_f32 v[30:31], v[30:31], s[76:77], v[230:231] op_sel_hi:[1,0,0]
	v_pk_fma_f32 v[32:33], v[68:69], s[74:75], v[12:13] op_sel_hi:[1,0,1] clamp
	v_exp_f32_e32 v68, v30
	v_cvt_pk_fp8_f32 v4, v28, v29 op_sel:[0,0,1]
	v_pk_fma_f32 v[28:29], v[72:73], s[98:99], v[8:9] op_sel_hi:[1,0,1] clamp
	v_exp_f32_e32 v69, v31
	v_pk_fma_f32 v[28:29], v[28:29], s[76:77], v[230:231] op_sel_hi:[1,0,0]
	v_exp_f32_e32 v70, v28
	v_exp_f32_e32 v71, v29
	v_pk_fma_f32 v[68:69], v[68:69], s[96:97], s[96:97] op_sel_hi:[1,0,0]
	v_pk_fma_f32 v[66:67], v[66:67], s[74:75], v[14:15] op_sel_hi:[1,0,1] clamp
	v_rcp_f32_e32 v68, v68
	v_rcp_f32_e32 v69, v69
	v_pk_fma_f32 v[66:67], v[66:67], s[64:65], v[186:187] op_sel_hi:[1,0,0]
	v_pk_fma_f32 v[70:71], v[70:71], s[96:97], s[96:97] op_sel_hi:[1,0,0]
	v_pk_mul_f32 v[30:31], v[30:31], v[66:67]
	v_rcp_f32_e32 v70, v70
	v_rcp_f32_e32 v71, v71
	v_pk_mul_f32 v[30:31], v[30:31], v[68:69]
	v_cvt_pk_fp8_f32 v5, v30, v31
	v_pk_fma_f32 v[32:33], v[32:33], s[64:65], v[186:187] op_sel_hi:[1,0,0]
	v_pk_mul_f32 v[28:29], v[28:29], v[32:33]
	v_pk_fma_f32 v[30:31], v[62:63], s[98:99], v[18:19] op_sel_hi:[1,0,1] clamp
	v_pk_mul_f32 v[28:29], v[28:29], v[70:71]
	v_pk_fma_f32 v[32:33], v[60:61], s[74:75], v[20:21] op_sel_hi:[1,0,1] clamp
	v_cvt_pk_fp8_f32 v5, v28, v29 op_sel:[0,0,1]
	v_pk_fma_f32 v[28:29], v[64:65], s[98:99], v[16:17] op_sel_hi:[1,0,1] clamp
	v_pk_fma_f32 v[30:31], v[30:31], s[76:77], v[230:231] op_sel_hi:[1,0,0]
	v_pk_fma_f32 v[60:61], v[28:29], s[76:77], v[230:231] op_sel_hi:[1,0,0]
	v_exp_f32_e32 v28, v30
	v_exp_f32_e32 v62, v60
	v_exp_f32_e32 v63, v61
	v_exp_f32_e32 v29, v31
	v_pk_fma_f32 v[58:59], v[58:59], s[74:75], v[22:23] op_sel_hi:[1,0,1] clamp
	v_pk_fma_f32 v[32:33], v[32:33], s[64:65], v[186:187] op_sel_hi:[1,0,0]
	v_pk_fma_f32 v[58:59], v[58:59], s[64:65], v[186:187] op_sel_hi:[1,0,0]
	v_pk_fma_f32 v[28:29], v[28:29], s[96:97], s[96:97] op_sel_hi:[1,0,0]
	v_rcp_f32_e32 v28, v28
	v_rcp_f32_e32 v29, v29
	v_pk_fma_f32 v[62:63], v[62:63], s[96:97], s[96:97] op_sel_hi:[1,0,0]
	v_pk_mul_f32 v[30:31], v[30:31], v[58:59]
	v_rcp_f32_e32 v62, v62
	v_rcp_f32_e32 v63, v63
	v_pk_mul_f32 v[30:31], v[30:31], v[28:29]
	v_cvt_pk_fp8_f32 v28, v30, v31
	v_pk_mul_f32 v[30:31], v[60:61], v[32:33]
	v_pk_fma_f32 v[32:33], v[54:55], s[98:99], v[10:11] op_sel_hi:[1,0,1] clamp
	v_pk_mul_f32 v[30:31], v[30:31], v[62:63]
	v_pk_fma_f32 v[32:33], v[32:33], s[76:77], v[230:231] op_sel_hi:[1,0,0]
	v_exp_f32_e32 v54, v32
	v_cvt_pk_fp8_f32 v28, v30, v31 op_sel:[0,0,1]
	v_pk_fma_f32 v[30:31], v[56:57], s[98:99], v[8:9] op_sel_hi:[1,0,1] clamp
	v_exp_f32_e32 v55, v33
	v_pk_fma_f32 v[30:31], v[30:31], s[76:77], v[230:231] op_sel_hi:[1,0,0]
	v_exp_f32_e32 v56, v30
	v_exp_f32_e32 v57, v31
	v_pk_fma_f32 v[54:55], v[54:55], s[96:97], s[96:97] op_sel_hi:[1,0,0]
	v_pk_fma_f32 v[50:51], v[50:51], s[74:75], v[14:15] op_sel_hi:[1,0,1] clamp
	v_rcp_f32_e32 v54, v54
	v_rcp_f32_e32 v55, v55
	v_pk_fma_f32 v[50:51], v[50:51], s[64:65], v[186:187] op_sel_hi:[1,0,0]
	v_pk_fma_f32 v[56:57], v[56:57], s[96:97], s[96:97] op_sel_hi:[1,0,0]
	v_pk_mul_f32 v[32:33], v[32:33], v[50:51]
	v_rcp_f32_e32 v56, v56
	v_rcp_f32_e32 v57, v57
	v_pk_mul_f32 v[32:33], v[32:33], v[54:55]
	v_pk_fma_f32 v[52:53], v[52:53], s[74:75], v[12:13] op_sel_hi:[1,0,1] clamp
	v_cvt_pk_fp8_f32 v29, v32, v33
	v_pk_fma_f32 v[52:53], v[52:53], s[64:65], v[186:187] op_sel_hi:[1,0,0]
	v_pk_mul_f32 v[30:31], v[30:31], v[52:53]
	v_pk_fma_f32 v[16:17], v[48:49], s[98:99], v[16:17] op_sel_hi:[1,0,1] clamp
	v_pk_fma_f32 v[18:19], v[46:47], s[98:99], v[18:19] op_sel_hi:[1,0,1] clamp
	v_pk_mul_f32 v[30:31], v[30:31], v[56:57]
	v_pk_fma_f32 v[18:19], v[18:19], s[76:77], v[230:231] op_sel_hi:[1,0,0]
	v_pk_fma_f32 v[16:17], v[16:17], s[76:77], v[230:231] op_sel_hi:[1,0,0]
	v_cvt_pk_fp8_f32 v29, v30, v31 op_sel:[0,0,1]
	v_exp_f32_e32 v30, v18
	v_exp_f32_e32 v32, v16
	v_exp_f32_e32 v33, v17
	v_exp_f32_e32 v31, v19
	v_pk_fma_f32 v[22:23], v[42:43], s[74:75], v[22:23] op_sel_hi:[1,0,1] clamp
	v_pk_fma_f32 v[20:21], v[44:45], s[74:75], v[20:21] op_sel_hi:[1,0,1] clamp
	v_pk_fma_f32 v[22:23], v[22:23], s[64:65], v[186:187] op_sel_hi:[1,0,0]
	v_pk_fma_f32 v[30:31], v[30:31], s[96:97], s[96:97] op_sel_hi:[1,0,0]
	v_rcp_f32_e32 v30, v30
	v_rcp_f32_e32 v31, v31
	v_pk_fma_f32 v[32:33], v[32:33], s[96:97], s[96:97] op_sel_hi:[1,0,0]
	v_pk_mul_f32 v[18:19], v[18:19], v[22:23]
	v_rcp_f32_e32 v32, v32
	v_rcp_f32_e32 v33, v33
	v_pk_mul_f32 v[18:19], v[18:19], v[30:31]
	v_cvt_pk_fp8_f32 v30, v18, v19
	v_pk_fma_f32 v[20:21], v[20:21], s[64:65], v[186:187] op_sel_hi:[1,0,0]
	v_pk_mul_f32 v[16:17], v[16:17], v[20:21]
	v_pk_fma_f32 v[10:11], v[38:39], s[98:99], v[10:11] op_sel_hi:[1,0,1] clamp
	v_pk_mul_f32 v[16:17], v[16:17], v[32:33]
	v_pk_fma_f32 v[10:11], v[10:11], s[76:77], v[230:231] op_sel_hi:[1,0,0]
	v_cvt_pk_fp8_f32 v30, v16, v17 op_sel:[0,0,1]
	v_exp_f32_e32 v16, v10
	v_exp_f32_e32 v17, v11
	v_pk_fma_f32 v[8:9], v[40:41], s[98:99], v[8:9] op_sel_hi:[1,0,1] clamp
	v_pk_fma_f32 v[14:15], v[34:35], s[74:75], v[14:15] op_sel_hi:[1,0,1] clamp
	v_pk_fma_f32 v[8:9], v[8:9], s[76:77], v[230:231] op_sel_hi:[1,0,0]
	v_exp_f32_e32 v18, v8
	v_exp_f32_e32 v19, v9
	v_pk_fma_f32 v[16:17], v[16:17], s[96:97], s[96:97] op_sel_hi:[1,0,0]
	v_pk_fma_f32 v[14:15], v[14:15], s[64:65], v[186:187] op_sel_hi:[1,0,0]
	v_rcp_f32_e32 v16, v16
	v_rcp_f32_e32 v17, v17
	v_pk_fma_f32 v[18:19], v[18:19], s[96:97], s[96:97] op_sel_hi:[1,0,0]
	v_pk_mul_f32 v[10:11], v[10:11], v[14:15]
	v_rcp_f32_e32 v18, v18
	v_rcp_f32_e32 v19, v19
	v_pk_mul_f32 v[10:11], v[10:11], v[16:17]
	v_pk_fma_f32 v[12:13], v[36:37], s[74:75], v[12:13] op_sel_hi:[1,0,1] clamp
	v_cvt_pk_fp8_f32 v31, v10, v11
	v_pk_fma_f32 v[12:13], v[12:13], s[64:65], v[186:187] op_sel_hi:[1,0,0]
	v_pk_mul_f32 v[8:9], v[8:9], v[12:13]
	v_add_u32_e32 v10, 0x80, v24
	v_pk_mul_f32 v[8:9], v[8:9], v[18:19]
	v_permlane16_swap_b32_e32 v2, v4
	v_cvt_pk_fp8_f32 v31, v8, v9 op_sel:[0,0,1]
	v_or_b32_e32 v8, v10, v25
	v_ashrrev_i32_e32 v9, 31, v8
	v_lshlrev_b64 v[8:9], 10, v[8:9]
	v_lshl_add_u64 v[8:9], s[12:13], 0, v[8:9]
	v_lshl_add_u64 v[8:9], v[8:9], 0, s[38:39]
	v_lshl_add_u64 v[8:9], v[8:9], 0, v[162:163]
	v_permlane16_swap_b32_e32 v3, v5
	v_lshl_add_u64 v[8:9], v[8:9], 0, v[6:7]
	global_store_dwordx4 v[8:9], v[2:5], off
	v_permlane16_swap_b32_e32 v28, v30
	s_nop 0
	v_or_b32_e32 v2, v10, v26
	v_ashrrev_i32_e32 v3, 31, v2
	v_lshlrev_b64 v[2:3], 10, v[2:3]
	v_lshl_add_u64 v[2:3], s[12:13], 0, v[2:3]
	v_lshl_add_u64 v[2:3], v[2:3], 0, s[38:39]
	v_lshl_add_u64 v[2:3], v[2:3], 0, v[162:163]
	v_permlane16_swap_b32_e32 v29, v31
	v_lshl_add_u64 v[2:3], v[2:3], 0, v[6:7]
	s_and_b64 vcc, exec, s[4:5]
	s_mov_b64 s[4:5], -1
	global_store_dwordx4 v[2:3], v[28:31], off
	s_cbranch_vccnz .LBB0_557
	s_andn2_b64 vcc, exec, s[16:17]
	s_cbranch_vccnz .LBB0_569
	s_lshl_b32 s4, s66, 10
	s_and_b32 s4, s4, 0x400
	s_add_i32 s4, s4, 0
	s_ashr_i32 s37, s36, 31
	s_add_i32 s35, s4, 0x24cc0
	s_lshl_b64 s[4:5], s[36:37], 13
	s_add_u32 s37, s14, s4
	s_addc_u32 s38, s15, s5
	s_lshl_b32 s4, s36, 10
	s_lshl_b32 s5, s34, 7
	s_sub_i32 s4, s5, s4
	s_ashr_i32 s5, s4, 31
	s_lshl_b64 s[4:5], s[4:5], 2
	s_add_u32 s4, s37, s4
	s_addc_u32 s5, s38, s5
	s_mov_b32 m0, s35
	s_nop 0
	global_load_lds_dwordx4 v178, s[4:5] offset:0
